# stack + second s_nop 15 after each fp8 K-loop dropped
# speedup vs baseline: 1.0104x; 1.0015x over previous
.LBB0_1544:
	s_nop 15
	s_andn2_b64 vcc, exec, s[26:27]
	s_cbranch_vccnz .LBB0_1546
	s_barrier

.LBB0_1625:
	s_nop 15
	s_andn2_b64 vcc, exec, s[10:11]
	s_cbranch_vccnz .LBB0_1627
	s_barrier

.LBB0_1778:
	s_nop 15
	s_andn2_b64 vcc, exec, s[20:21]
	s_cbranch_vccnz .LBB0_1780
	s_barrier

.LBB0_1848:
	s_nop 15
	s_andn2_b64 vcc, exec, s[28:29]
	s_cbranch_vccnz .LBB0_1850
	s_barrier

.LBB0_2300:
	s_nop 15
	s_andn2_b64 vcc, exec, s[18:19]
	s_cbranch_vccnz .LBB0_2302
	s_barrier
